# ssm_final: inputs also staged as f32, 16-step block unrolled by hand with prefetched inputs and tail/FMA interleave (21 VALU per step)
# speedup vs baseline: 1.0143x; 1.0143x over previous
.LBB0_531:
	s_or_b64 exec, exec, s[0:1]
	v_add_f32_e32 v75, -1.0, v72
	v_mov_b32_e32 v86, v77
	v_pk_mul_f32 v[84:85], v[76:77], v[76:77]
	v_pk_mul_f32 v[86:87], v[86:87], v[74:75] op_sel:[0,1] op_sel_hi:[0,0]
	v_pk_fma_f32 v[88:89], v[76:77], v[74:75], v[86:87] op_sel_hi:[0,1,1]
	v_pk_add_f32 v[84:85], v[84:85], v[84:85] op_sel:[0,1] op_sel_hi:[0,1]
	v_div_scale_f32 v71, s[0:1], v85, v85, v89
	v_rcp_f32_e32 v73, v71
	v_pk_fma_f32 v[76:77], v[76:77], v[74:75], v[86:87] op_sel_hi:[0,1,1] neg_lo:[0,0,1] neg_hi:[0,0,1]
	s_waitcnt vmcnt(0) lgkmcnt(0)
	v_mul_f32_e32 v101, v93, v0
	v_mul_hi_i32 v0, v90, s78
	v_fma_f32 v75, -v71, v73, 1.0
	v_fmac_f32_e32 v73, v75, v73
	v_div_scale_f32 v75, vcc, v89, v85, v89
	v_mul_f32_e32 v77, v75, v73
	v_fma_f32 v81, -v71, v77, v75
	v_fmac_f32_e32 v77, v81, v73
	v_fma_f32 v71, -v71, v77, v75
	v_div_fmas_f32 v71, v71, v73, v77
	v_div_fixup_f32 v85, v71, v85, v89
	v_div_scale_f32 v71, s[0:1], v84, v84, v76
	v_rcp_f32_e32 v73, v71
	v_add_u32_e32 v0, v0, v90
	v_mul_f32_e32 v102, v93, v1
	v_lshrrev_b32_e32 v1, 31, v0
	v_fma_f32 v75, -v71, v73, 1.0
	v_fmac_f32_e32 v73, v75, v73
	v_div_scale_f32 v75, vcc, v76, v84, v76
	v_mul_f32_e32 v77, v75, v73
	v_fma_f32 v81, -v71, v77, v75
	v_fmac_f32_e32 v77, v81, v73
	v_fma_f32 v71, -v71, v77, v75
	v_div_fmas_f32 v71, v71, v73, v77
	v_div_fixup_f32 v84, v71, v84, v76
	v_pk_mul_f32 v[76:77], v[60:61], v[84:85] op_sel:[0,1] op_sel_hi:[0,0]
	v_pk_fma_f32 v[86:87], v[56:57], v[84:85], v[76:77] op_sel_hi:[0,1,1] neg_lo:[0,0,1] neg_hi:[0,0,1]
	v_pk_fma_f32 v[76:77], v[56:57], v[84:85], v[76:77] op_sel_hi:[0,1,1]
	v_pk_mul_f32 v[60:61], v[60:61], v[84:85] op_sel:[1,1] op_sel_hi:[1,0]
	v_mov_b32_e32 v77, v87
	v_pk_fma_f32 v[86:87], v[56:57], v[84:85], v[60:61] op_sel:[1,0,0] neg_lo:[0,0,1] neg_hi:[0,0,1]
	v_pk_fma_f32 v[56:57], v[56:57], v[84:85], v[60:61] op_sel:[1,0,0]
	v_pk_mul_f32 v[60:61], v[62:63], v[84:85] op_sel:[0,1] op_sel_hi:[0,0]
	v_mov_b32_e32 v57, v87
	v_pk_fma_f32 v[86:87], v[58:59], v[84:85], v[60:61] op_sel_hi:[0,1,1] neg_lo:[0,0,1] neg_hi:[0,0,1]
	v_pk_fma_f32 v[60:61], v[58:59], v[84:85], v[60:61] op_sel_hi:[0,1,1]
	v_mov_b32_e32 v58, v63
	v_pk_mul_f32 v[62:63], v[58:59], v[84:85] op_sel:[0,1] op_sel_hi:[0,0]
	v_mov_b32_e32 v58, v59
	v_mov_b32_e32 v61, v87
	v_pk_fma_f32 v[86:87], v[58:59], v[84:85], v[62:63] op_sel_hi:[0,1,1] neg_lo:[0,0,1] neg_hi:[0,0,1]
	v_pk_fma_f32 v[58:59], v[58:59], v[84:85], v[62:63] op_sel_hi:[0,1,1]
	v_pk_mul_f32 v[62:63], v[84:85], v[52:53] op_sel:[1,0] op_sel_hi:[0,0]
	v_mov_b32_e32 v59, v87
	v_pk_fma_f32 v[86:87], v[48:49], v[84:85], v[62:63] op_sel_hi:[0,1,1] neg_lo:[0,0,1] neg_hi:[0,0,1]
	v_pk_fma_f32 v[62:63], v[48:49], v[84:85], v[62:63] op_sel_hi:[0,1,1]
	v_pk_mul_f32 v[52:53], v[84:85], v[52:53] op_sel:[1,1] op_sel_hi:[0,1]
	v_mov_b32_e32 v63, v87
	v_pk_fma_f32 v[86:87], v[48:49], v[84:85], v[52:53] op_sel:[1,0,0] neg_lo:[0,0,1] neg_hi:[0,0,1]
	v_pk_fma_f32 v[48:49], v[48:49], v[84:85], v[52:53] op_sel:[1,0,0]
	v_pk_mul_f32 v[52:53], v[84:85], v[54:55] op_sel:[1,0] op_sel_hi:[0,0]
	v_mov_b32_e32 v49, v87
	v_pk_fma_f32 v[86:87], v[50:51], v[84:85], v[52:53] op_sel_hi:[0,1,1] neg_lo:[0,0,1] neg_hi:[0,0,1]
	v_pk_fma_f32 v[52:53], v[50:51], v[84:85], v[52:53] op_sel_hi:[0,1,1]
	v_mov_b32_e32 v50, v55
	v_pk_mul_f32 v[54:55], v[84:85], v[50:51] op_sel:[1,0] op_sel_hi:[0,0]
	v_mov_b32_e32 v50, v51
	v_mov_b32_e32 v53, v87
	v_pk_fma_f32 v[86:87], v[50:51], v[84:85], v[54:55] op_sel_hi:[0,1,1] neg_lo:[0,0,1] neg_hi:[0,0,1]
	v_pk_fma_f32 v[50:51], v[50:51], v[84:85], v[54:55] op_sel_hi:[0,1,1]
	v_pk_mul_f32 v[54:55], v[84:85], v[44:45] op_sel:[1,0] op_sel_hi:[0,0]
	v_mov_b32_e32 v51, v87
	v_pk_fma_f32 v[86:87], v[84:85], v[40:41], v[54:55] op_sel_hi:[1,0,1] neg_lo:[0,0,1] neg_hi:[0,0,1]
	v_pk_fma_f32 v[54:55], v[84:85], v[40:41], v[54:55] op_sel_hi:[1,0,1]
	v_pk_mul_f32 v[44:45], v[84:85], v[44:45] op_sel:[1,1] op_sel_hi:[0,1]
	v_mov_b32_e32 v55, v87
	v_pk_fma_f32 v[86:87], v[84:85], v[40:41], v[44:45] op_sel:[0,1,0] neg_lo:[0,0,1] neg_hi:[0,0,1]
	v_pk_fma_f32 v[40:41], v[84:85], v[40:41], v[44:45] op_sel:[0,1,0]
	v_pk_mul_f32 v[44:45], v[84:85], v[46:47] op_sel:[1,0] op_sel_hi:[0,0]
	v_mov_b32_e32 v41, v87
	v_pk_fma_f32 v[86:87], v[84:85], v[42:43], v[44:45] op_sel_hi:[1,0,1] neg_lo:[0,0,1] neg_hi:[0,0,1]
	v_pk_fma_f32 v[44:45], v[84:85], v[42:43], v[44:45] op_sel_hi:[1,0,1]
	v_mov_b32_e32 v42, v47
	v_pk_mul_f32 v[46:47], v[84:85], v[42:43] op_sel:[1,0] op_sel_hi:[0,0]
	v_mov_b32_e32 v42, v43
	v_mov_b32_e32 v45, v87
	v_pk_fma_f32 v[86:87], v[84:85], v[42:43], v[46:47] op_sel_hi:[1,0,1] neg_lo:[0,0,1] neg_hi:[0,0,1]
	v_pk_fma_f32 v[42:43], v[84:85], v[42:43], v[46:47] op_sel_hi:[1,0,1]
	v_pk_mul_f32 v[46:47], v[84:85], v[36:37] op_sel:[1,0] op_sel_hi:[0,0]
	v_mov_b32_e32 v43, v87
	v_pk_fma_f32 v[86:87], v[84:85], v[24:25], v[46:47] op_sel_hi:[1,0,1] neg_lo:[0,0,1] neg_hi:[0,0,1]
	v_pk_fma_f32 v[46:47], v[84:85], v[24:25], v[46:47] op_sel_hi:[1,0,1]
	v_pk_mul_f32 v[36:37], v[84:85], v[36:37] op_sel:[1,1] op_sel_hi:[0,1]
	v_ashrrev_i32_e32 v0, 9, v0
	v_mov_b32_e32 v47, v87
	v_pk_fma_f32 v[86:87], v[84:85], v[24:25], v[36:37] op_sel:[0,1,0] neg_lo:[0,0,1] neg_hi:[0,0,1]
	v_pk_fma_f32 v[24:25], v[84:85], v[24:25], v[36:37] op_sel:[0,1,0]
	v_pk_mul_f32 v[36:37], v[84:85], v[38:39] op_sel:[1,0] op_sel_hi:[0,0]
	v_add_u32_e32 v0, v0, v1
	v_mov_b32_e32 v25, v87
	v_pk_fma_f32 v[86:87], v[84:85], v[26:27], v[36:37] op_sel_hi:[1,0,1] neg_lo:[0,0,1] neg_hi:[0,0,1]
	v_pk_fma_f32 v[36:37], v[84:85], v[26:27], v[36:37] op_sel_hi:[1,0,1]
	v_mov_b32_e32 v26, v39
	v_ashrrev_i32_e32 v1, 31, v0
	v_ashrrev_i32_e32 v83, 31, v82
	v_pk_mul_f32 v[38:39], v[84:85], v[26:27] op_sel:[1,0] op_sel_hi:[0,0]
	v_mov_b32_e32 v26, v27
	v_mul_f32_e32 v103, v93, v2
	v_mul_f32_e32 v104, v93, v3
	v_lshlrev_b64 v[0:1], 11, v[0:1]
	v_lshlrev_b64 v[2:3], 6, v[82:83]
	v_mov_b32_e32 v37, v87
	v_pk_fma_f32 v[86:87], v[84:85], v[26:27], v[38:39] op_sel_hi:[1,0,1] neg_lo:[0,0,1] neg_hi:[0,0,1]
	v_pk_fma_f32 v[26:27], v[84:85], v[26:27], v[38:39] op_sel_hi:[1,0,1]
	v_mul_f32_e32 v38, v93, v8
	v_mul_f32_e32 v39, v93, v9
	v_lshl_add_u64 v[8:9], v[0:1], 0, v[2:3]
	v_mov_b64_e32 v[0:1], s[10:11]
	v_mad_u64_u32 v[0:1], s[0:1], v8, s80, v[0:1]
	v_ashrrev_i32_e32 v81, 31, v80
	v_mul_f32_e32 v84, v93, v10
	v_mul_f32_e32 v85, v93, v11
	v_mad_i32_i24 v1, v9, s80, v1
	v_lshlrev_b64 v[10:11], 1, v[80:81]
	v_lshl_add_u64 v[0:1], v[0:1], 0, v[10:11]
	v_mov_b32_e32 v71, v145
	v_mov_b32_e32 v27, v87
	v_mul_f32_e32 v86, v93, v4
	v_mul_f32_e32 v87, v93, v5
	v_lshl_add_u64 v[4:5], v[0:1], 0, v[70:71]
	v_mul_f32_e32 v88, v93, v6
	v_mul_f32_e32 v89, v93, v7
	global_load_dwordx4 v[0:3], v[4:5], off offset:2704
	s_nop 0
	global_load_dwordx4 v[4:7], v[4:5], off offset:2688
	s_waitcnt vmcnt(0)
	ds_write_b128 v98, v[4:7]
	ds_write_b128 v98, v[0:3] offset:16
	v_lshlrev_b32_e32 v132, 1, v97
	v_add_u32_e32 v132, 0x14800, v132
	v_lshl_add_u32 v134, v91, 6, v132
	v_lshlrev_b32_e32 v146, 16, v4
	v_and_b32_e32 v147, 0xffff0000, v4
	v_lshlrev_b32_e32 v148, 16, v5
	v_and_b32_e32 v149, 0xffff0000, v5
	v_lshlrev_b32_e32 v150, 16, v6
	v_and_b32_e32 v151, 0xffff0000, v6
	v_lshlrev_b32_e32 v152, 16, v7
	v_and_b32_e32 v153, 0xffff0000, v7
	v_lshlrev_b32_e32 v154, 16, v0
	v_and_b32_e32 v155, 0xffff0000, v0
	v_lshlrev_b32_e32 v156, 16, v1
	v_and_b32_e32 v157, 0xffff0000, v1
	v_lshlrev_b32_e32 v158, 16, v2
	v_and_b32_e32 v159, 0xffff0000, v2
	v_lshlrev_b32_e32 v160, 16, v3
	v_and_b32_e32 v161, 0xffff0000, v3
	ds_write_b128 v134, v[146:149]
	ds_write_b128 v134, v[150:153] offset:16
	ds_write_b128 v134, v[154:157] offset:32
	ds_write_b128 v134, v[158:161] offset:48
	s_waitcnt lgkmcnt(0)
	v_mul_f32_e32 v32, v93, v32
	v_mul_f32_e32 v33, v93, v33
	v_mul_f32_e32 v34, v93, v34
	v_mul_f32_e32 v35, v93, v35
	v_mul_f32_e32 v28, v93, v28
	v_mul_f32_e32 v29, v93, v29
	v_mul_f32_e32 v30, v93, v30
	v_mul_f32_e32 v31, v93, v31
	v_mul_f32_e32 v20, v93, v20
	v_mul_f32_e32 v21, v93, v21
	v_mul_f32_e32 v22, v93, v22
	v_mul_f32_e32 v23, v93, v23
	v_mul_f32_e32 v16, v93, v16
	v_mul_f32_e32 v17, v93, v17
	v_mul_f32_e32 v18, v93, v18
	v_mul_f32_e32 v19, v93, v19
	v_mul_f32_e32 v12, v93, v12
	v_mul_f32_e32 v13, v93, v13
	v_mul_f32_e32 v14, v93, v14
	v_mul_f32_e32 v15, v93, v15
	v_xor_b32_e32 v75, 0x80000000, v74
	v_lshl_add_u64 v[0:1], v[80:81], 2, v[66:67]
	v_lshl_add_u64 v[2:3], v[68:69], 0, v[10:11]
	v_mov_b32_e32 v73, v72
	s_mov_b32 s0, 0
	v_mov_b32_e32 v6, v97
.LBB0_532:
	v_lshl_add_u32 v133, s0, 10, v132
	ds_read_b128 v[146:149], v133
	ds_read_b128 v[150:153], v133 offset:16
	ds_read_b128 v[154:157], v133 offset:32
	ds_read_b128 v[158:161], v133 offset:48
	ds_read_b128 v[162:165], v133 offset:64
	ds_read_b128 v[166:169], v133 offset:80
	ds_read_b128 v[170:173], v133 offset:96
	ds_read_b128 v[174:177], v133 offset:112
	s_waitcnt lgkmcnt(4)
	v_pk_fma_f32 v[178:179], v[146:147], v[76:77], 0 op_sel_hi:[0,1,0]
	v_pk_fma_f32 v[180:181], v[146:147], v[56:57], 0 op_sel:[1,0,0] op_sel_hi:[1,1,0]
	v_pk_fma_f32 v[182:183], v[148:149], v[60:61], 0 op_sel_hi:[0,1,0]
	v_pk_fma_f32 v[184:185], v[148:149], v[58:59], 0 op_sel:[1,0,0] op_sel_hi:[1,1,0]
	v_pk_fma_f32 v[178:179], v[150:151], v[62:63], v[178:179] op_sel_hi:[0,1,1]
	v_pk_fma_f32 v[180:181], v[150:151], v[48:49], v[180:181] op_sel:[1,0,0]
	v_pk_fma_f32 v[182:183], v[152:153], v[52:53], v[182:183] op_sel_hi:[0,1,1]
	v_pk_fma_f32 v[184:185], v[152:153], v[50:51], v[184:185] op_sel:[1,0,0]
	v_pk_fma_f32 v[178:179], v[154:155], v[54:55], v[178:179] op_sel_hi:[0,1,1]
	v_pk_fma_f32 v[180:181], v[154:155], v[40:41], v[180:181] op_sel:[1,0,0]
	v_pk_fma_f32 v[182:183], v[156:157], v[44:45], v[182:183] op_sel_hi:[0,1,1]
	v_pk_fma_f32 v[184:185], v[156:157], v[42:43], v[184:185] op_sel:[1,0,0]
	v_pk_fma_f32 v[178:179], v[158:159], v[46:47], v[178:179] op_sel_hi:[0,1,1]
	v_pk_fma_f32 v[180:181], v[158:159], v[24:25], v[180:181] op_sel:[1,0,0]
	v_pk_fma_f32 v[182:183], v[160:161], v[36:37], v[182:183] op_sel_hi:[0,1,1]
	v_pk_fma_f32 v[184:185], v[160:161], v[26:27], v[184:185] op_sel:[1,0,0]
	ds_read_b128 v[146:149], v133 offset:128
	ds_read_b128 v[150:153], v133 offset:144
	ds_read_b128 v[154:157], v133 offset:160
	ds_read_b128 v[158:161], v133 offset:176
	s_waitcnt lgkmcnt(4)
	v_pk_fma_f32 v[186:187], v[162:163], v[76:77], 0 op_sel_hi:[0,1,0]
	v_pk_add_f32 v[178:179], v[178:179], v[180:181]
	v_pk_fma_f32 v[188:189], v[162:163], v[56:57], 0 op_sel:[1,0,0] op_sel_hi:[1,1,0]
	v_pk_add_f32 v[182:183], v[182:183], v[184:185]
	v_pk_fma_f32 v[190:191], v[164:165], v[60:61], 0 op_sel_hi:[0,1,0]
	v_pk_add_f32 v[178:179], v[178:179], v[182:183]
	v_pk_fma_f32 v[192:193], v[164:165], v[58:59], 0 op_sel:[1,0,0] op_sel_hi:[1,1,0]
	v_pk_fma_f32 v[178:179], v[74:75], v[78:79], v[178:179] op_sel:[0,1,0] op_sel_hi:[1,0,1]
	v_pk_fma_f32 v[186:187], v[166:167], v[62:63], v[186:187] op_sel_hi:[0,1,1]
	v_pk_fma_f32 v[78:79], v[72:73], v[78:79], v[178:179]
	v_pk_fma_f32 v[188:189], v[166:167], v[48:49], v[188:189] op_sel:[1,0,0]
	ds_write_b32 v94, v79
	ds_write_b32 v94, v78 offset:256
	v_pk_fma_f32 v[190:191], v[168:169], v[52:53], v[190:191] op_sel_hi:[0,1,1]
	v_pk_fma_f32 v[192:193], v[168:169], v[50:51], v[192:193] op_sel:[1,0,0]
	v_pk_fma_f32 v[186:187], v[170:171], v[54:55], v[186:187] op_sel_hi:[0,1,1]
	v_pk_fma_f32 v[188:189], v[170:171], v[40:41], v[188:189] op_sel:[1,0,0]
	v_pk_fma_f32 v[190:191], v[172:173], v[44:45], v[190:191] op_sel_hi:[0,1,1]
	v_pk_fma_f32 v[192:193], v[172:173], v[42:43], v[192:193] op_sel:[1,0,0]
	v_pk_fma_f32 v[186:187], v[174:175], v[46:47], v[186:187] op_sel_hi:[0,1,1]
	v_pk_fma_f32 v[188:189], v[174:175], v[24:25], v[188:189] op_sel:[1,0,0]
	v_pk_fma_f32 v[190:191], v[176:177], v[36:37], v[190:191] op_sel_hi:[0,1,1]
	v_pk_fma_f32 v[192:193], v[176:177], v[26:27], v[192:193] op_sel:[1,0,0]
	ds_read_b128 v[162:165], v133 offset:192
	ds_read_b128 v[166:169], v133 offset:208
	ds_read_b128 v[170:173], v133 offset:224
	ds_read_b128 v[174:177], v133 offset:240
	s_waitcnt lgkmcnt(4)
	v_pk_fma_f32 v[178:179], v[146:147], v[76:77], 0 op_sel_hi:[0,1,0]
	v_pk_add_f32 v[186:187], v[186:187], v[188:189]
	v_pk_fma_f32 v[180:181], v[146:147], v[56:57], 0 op_sel:[1,0,0] op_sel_hi:[1,1,0]
	v_pk_add_f32 v[190:191], v[190:191], v[192:193]
	v_pk_fma_f32 v[182:183], v[148:149], v[60:61], 0 op_sel_hi:[0,1,0]
	v_pk_add_f32 v[186:187], v[186:187], v[190:191]
	v_pk_fma_f32 v[184:185], v[148:149], v[58:59], 0 op_sel:[1,0,0] op_sel_hi:[1,1,0]
	v_pk_fma_f32 v[186:187], v[74:75], v[78:79], v[186:187] op_sel:[0,1,0] op_sel_hi:[1,0,1]
	v_pk_fma_f32 v[178:179], v[150:151], v[62:63], v[178:179] op_sel_hi:[0,1,1]
	v_pk_fma_f32 v[78:79], v[72:73], v[78:79], v[186:187]
	v_pk_fma_f32 v[180:181], v[150:151], v[48:49], v[180:181] op_sel:[1,0,0]
	ds_write_b32 v94, v79 offset:528
	ds_write_b32 v94, v78 offset:784
	v_pk_fma_f32 v[182:183], v[152:153], v[52:53], v[182:183] op_sel_hi:[0,1,1]
	v_pk_fma_f32 v[184:185], v[152:153], v[50:51], v[184:185] op_sel:[1,0,0]
	v_pk_fma_f32 v[178:179], v[154:155], v[54:55], v[178:179] op_sel_hi:[0,1,1]
	v_pk_fma_f32 v[180:181], v[154:155], v[40:41], v[180:181] op_sel:[1,0,0]
	v_pk_fma_f32 v[182:183], v[156:157], v[44:45], v[182:183] op_sel_hi:[0,1,1]
	v_pk_fma_f32 v[184:185], v[156:157], v[42:43], v[184:185] op_sel:[1,0,0]
	v_pk_fma_f32 v[178:179], v[158:159], v[46:47], v[178:179] op_sel_hi:[0,1,1]
	v_pk_fma_f32 v[180:181], v[158:159], v[24:25], v[180:181] op_sel:[1,0,0]
	v_pk_fma_f32 v[182:183], v[160:161], v[36:37], v[182:183] op_sel_hi:[0,1,1]
	v_pk_fma_f32 v[184:185], v[160:161], v[26:27], v[184:185] op_sel:[1,0,0]
	ds_read_b128 v[146:149], v133 offset:256
	ds_read_b128 v[150:153], v133 offset:272
	ds_read_b128 v[154:157], v133 offset:288
	ds_read_b128 v[158:161], v133 offset:304
	s_waitcnt lgkmcnt(4)
	v_pk_fma_f32 v[186:187], v[162:163], v[76:77], 0 op_sel_hi:[0,1,0]
	v_pk_add_f32 v[178:179], v[178:179], v[180:181]
	v_pk_fma_f32 v[188:189], v[162:163], v[56:57], 0 op_sel:[1,0,0] op_sel_hi:[1,1,0]
	v_pk_add_f32 v[182:183], v[182:183], v[184:185]
	v_pk_fma_f32 v[190:191], v[164:165], v[60:61], 0 op_sel_hi:[0,1,0]
	v_pk_add_f32 v[178:179], v[178:179], v[182:183]
	v_pk_fma_f32 v[192:193], v[164:165], v[58:59], 0 op_sel:[1,0,0] op_sel_hi:[1,1,0]
	v_pk_fma_f32 v[178:179], v[74:75], v[78:79], v[178:179] op_sel:[0,1,0] op_sel_hi:[1,0,1]
	v_pk_fma_f32 v[186:187], v[166:167], v[62:63], v[186:187] op_sel_hi:[0,1,1]
	v_pk_fma_f32 v[78:79], v[72:73], v[78:79], v[178:179]
	v_pk_fma_f32 v[188:189], v[166:167], v[48:49], v[188:189] op_sel:[1,0,0]
	ds_write_b32 v94, v79 offset:1056
	ds_write_b32 v94, v78 offset:1312
	v_pk_fma_f32 v[190:191], v[168:169], v[52:53], v[190:191] op_sel_hi:[0,1,1]
	v_pk_fma_f32 v[192:193], v[168:169], v[50:51], v[192:193] op_sel:[1,0,0]
	v_pk_fma_f32 v[186:187], v[170:171], v[54:55], v[186:187] op_sel_hi:[0,1,1]
	v_pk_fma_f32 v[188:189], v[170:171], v[40:41], v[188:189] op_sel:[1,0,0]
	v_pk_fma_f32 v[190:191], v[172:173], v[44:45], v[190:191] op_sel_hi:[0,1,1]
	v_pk_fma_f32 v[192:193], v[172:173], v[42:43], v[192:193] op_sel:[1,0,0]
	v_pk_fma_f32 v[186:187], v[174:175], v[46:47], v[186:187] op_sel_hi:[0,1,1]
	v_pk_fma_f32 v[188:189], v[174:175], v[24:25], v[188:189] op_sel:[1,0,0]
	v_pk_fma_f32 v[190:191], v[176:177], v[36:37], v[190:191] op_sel_hi:[0,1,1]
	v_pk_fma_f32 v[192:193], v[176:177], v[26:27], v[192:193] op_sel:[1,0,0]
	ds_read_b128 v[162:165], v133 offset:320
	ds_read_b128 v[166:169], v133 offset:336
	ds_read_b128 v[170:173], v133 offset:352
	ds_read_b128 v[174:177], v133 offset:368
	s_waitcnt lgkmcnt(4)
	v_pk_fma_f32 v[178:179], v[146:147], v[76:77], 0 op_sel_hi:[0,1,0]
	v_pk_add_f32 v[186:187], v[186:187], v[188:189]
	v_pk_fma_f32 v[180:181], v[146:147], v[56:57], 0 op_sel:[1,0,0] op_sel_hi:[1,1,0]
	v_pk_add_f32 v[190:191], v[190:191], v[192:193]
	v_pk_fma_f32 v[182:183], v[148:149], v[60:61], 0 op_sel_hi:[0,1,0]
	v_pk_add_f32 v[186:187], v[186:187], v[190:191]
	v_pk_fma_f32 v[184:185], v[148:149], v[58:59], 0 op_sel:[1,0,0] op_sel_hi:[1,1,0]
	v_pk_fma_f32 v[186:187], v[74:75], v[78:79], v[186:187] op_sel:[0,1,0] op_sel_hi:[1,0,1]
	v_pk_fma_f32 v[178:179], v[150:151], v[62:63], v[178:179] op_sel_hi:[0,1,1]
	v_pk_fma_f32 v[78:79], v[72:73], v[78:79], v[186:187]
	v_pk_fma_f32 v[180:181], v[150:151], v[48:49], v[180:181] op_sel:[1,0,0]
	ds_write_b32 v94, v79 offset:1584
	ds_write_b32 v94, v78 offset:1840
	v_pk_fma_f32 v[182:183], v[152:153], v[52:53], v[182:183] op_sel_hi:[0,1,1]
	v_pk_fma_f32 v[184:185], v[152:153], v[50:51], v[184:185] op_sel:[1,0,0]
	v_pk_fma_f32 v[178:179], v[154:155], v[54:55], v[178:179] op_sel_hi:[0,1,1]
	v_pk_fma_f32 v[180:181], v[154:155], v[40:41], v[180:181] op_sel:[1,0,0]
	v_pk_fma_f32 v[182:183], v[156:157], v[44:45], v[182:183] op_sel_hi:[0,1,1]
	v_pk_fma_f32 v[184:185], v[156:157], v[42:43], v[184:185] op_sel:[1,0,0]
	v_pk_fma_f32 v[178:179], v[158:159], v[46:47], v[178:179] op_sel_hi:[0,1,1]
	v_pk_fma_f32 v[180:181], v[158:159], v[24:25], v[180:181] op_sel:[1,0,0]
	v_pk_fma_f32 v[182:183], v[160:161], v[36:37], v[182:183] op_sel_hi:[0,1,1]
	v_pk_fma_f32 v[184:185], v[160:161], v[26:27], v[184:185] op_sel:[1,0,0]
	ds_read_b128 v[146:149], v133 offset:384
	ds_read_b128 v[150:153], v133 offset:400
	ds_read_b128 v[154:157], v133 offset:416
	ds_read_b128 v[158:161], v133 offset:432
	s_waitcnt lgkmcnt(4)
	v_pk_fma_f32 v[186:187], v[162:163], v[76:77], 0 op_sel_hi:[0,1,0]
	v_pk_add_f32 v[178:179], v[178:179], v[180:181]
	v_pk_fma_f32 v[188:189], v[162:163], v[56:57], 0 op_sel:[1,0,0] op_sel_hi:[1,1,0]
	v_pk_add_f32 v[182:183], v[182:183], v[184:185]
	v_pk_fma_f32 v[190:191], v[164:165], v[60:61], 0 op_sel_hi:[0,1,0]
	v_pk_add_f32 v[178:179], v[178:179], v[182:183]
	v_pk_fma_f32 v[192:193], v[164:165], v[58:59], 0 op_sel:[1,0,0] op_sel_hi:[1,1,0]
	v_pk_fma_f32 v[178:179], v[74:75], v[78:79], v[178:179] op_sel:[0,1,0] op_sel_hi:[1,0,1]
	v_pk_fma_f32 v[186:187], v[166:167], v[62:63], v[186:187] op_sel_hi:[0,1,1]
	v_pk_fma_f32 v[78:79], v[72:73], v[78:79], v[178:179]
	v_pk_fma_f32 v[188:189], v[166:167], v[48:49], v[188:189] op_sel:[1,0,0]
	ds_write_b32 v94, v79 offset:2112
	ds_write_b32 v94, v78 offset:2368
	v_pk_fma_f32 v[190:191], v[168:169], v[52:53], v[190:191] op_sel_hi:[0,1,1]
	v_pk_fma_f32 v[192:193], v[168:169], v[50:51], v[192:193] op_sel:[1,0,0]
	v_pk_fma_f32 v[186:187], v[170:171], v[54:55], v[186:187] op_sel_hi:[0,1,1]
	v_pk_fma_f32 v[188:189], v[170:171], v[40:41], v[188:189] op_sel:[1,0,0]
	v_pk_fma_f32 v[190:191], v[172:173], v[44:45], v[190:191] op_sel_hi:[0,1,1]
	v_pk_fma_f32 v[192:193], v[172:173], v[42:43], v[192:193] op_sel:[1,0,0]
	v_pk_fma_f32 v[186:187], v[174:175], v[46:47], v[186:187] op_sel_hi:[0,1,1]
	v_pk_fma_f32 v[188:189], v[174:175], v[24:25], v[188:189] op_sel:[1,0,0]
	v_pk_fma_f32 v[190:191], v[176:177], v[36:37], v[190:191] op_sel_hi:[0,1,1]
	v_pk_fma_f32 v[192:193], v[176:177], v[26:27], v[192:193] op_sel:[1,0,0]
	ds_read_b128 v[162:165], v133 offset:448
	ds_read_b128 v[166:169], v133 offset:464
	ds_read_b128 v[170:173], v133 offset:480
	ds_read_b128 v[174:177], v133 offset:496
	s_waitcnt lgkmcnt(4)
	v_pk_fma_f32 v[178:179], v[146:147], v[76:77], 0 op_sel_hi:[0,1,0]
	v_pk_add_f32 v[186:187], v[186:187], v[188:189]
	v_pk_fma_f32 v[180:181], v[146:147], v[56:57], 0 op_sel:[1,0,0] op_sel_hi:[1,1,0]
	v_pk_add_f32 v[190:191], v[190:191], v[192:193]
	v_pk_fma_f32 v[182:183], v[148:149], v[60:61], 0 op_sel_hi:[0,1,0]
	v_pk_add_f32 v[186:187], v[186:187], v[190:191]
	v_pk_fma_f32 v[184:185], v[148:149], v[58:59], 0 op_sel:[1,0,0] op_sel_hi:[1,1,0]
	v_pk_fma_f32 v[186:187], v[74:75], v[78:79], v[186:187] op_sel:[0,1,0] op_sel_hi:[1,0,1]
	v_pk_fma_f32 v[178:179], v[150:151], v[62:63], v[178:179] op_sel_hi:[0,1,1]
	v_pk_fma_f32 v[78:79], v[72:73], v[78:79], v[186:187]
	v_pk_fma_f32 v[180:181], v[150:151], v[48:49], v[180:181] op_sel:[1,0,0]
	ds_write_b32 v94, v79 offset:2640
	ds_write_b32 v94, v78 offset:2896
	v_pk_fma_f32 v[182:183], v[152:153], v[52:53], v[182:183] op_sel_hi:[0,1,1]
	v_pk_fma_f32 v[184:185], v[152:153], v[50:51], v[184:185] op_sel:[1,0,0]
	v_pk_fma_f32 v[178:179], v[154:155], v[54:55], v[178:179] op_sel_hi:[0,1,1]
	v_pk_fma_f32 v[180:181], v[154:155], v[40:41], v[180:181] op_sel:[1,0,0]
	v_pk_fma_f32 v[182:183], v[156:157], v[44:45], v[182:183] op_sel_hi:[0,1,1]
	v_pk_fma_f32 v[184:185], v[156:157], v[42:43], v[184:185] op_sel:[1,0,0]
	v_pk_fma_f32 v[178:179], v[158:159], v[46:47], v[178:179] op_sel_hi:[0,1,1]
	v_pk_fma_f32 v[180:181], v[158:159], v[24:25], v[180:181] op_sel:[1,0,0]
	v_pk_fma_f32 v[182:183], v[160:161], v[36:37], v[182:183] op_sel_hi:[0,1,1]
	v_pk_fma_f32 v[184:185], v[160:161], v[26:27], v[184:185] op_sel:[1,0,0]
	ds_read_b128 v[146:149], v133 offset:512
	ds_read_b128 v[150:153], v133 offset:528
	ds_read_b128 v[154:157], v133 offset:544
	ds_read_b128 v[158:161], v133 offset:560
	s_waitcnt lgkmcnt(4)
	v_pk_fma_f32 v[186:187], v[162:163], v[76:77], 0 op_sel_hi:[0,1,0]
	v_pk_add_f32 v[178:179], v[178:179], v[180:181]
	v_pk_fma_f32 v[188:189], v[162:163], v[56:57], 0 op_sel:[1,0,0] op_sel_hi:[1,1,0]
	v_pk_add_f32 v[182:183], v[182:183], v[184:185]
	v_pk_fma_f32 v[190:191], v[164:165], v[60:61], 0 op_sel_hi:[0,1,0]
	v_pk_add_f32 v[178:179], v[178:179], v[182:183]
	v_pk_fma_f32 v[192:193], v[164:165], v[58:59], 0 op_sel:[1,0,0] op_sel_hi:[1,1,0]
	v_pk_fma_f32 v[178:179], v[74:75], v[78:79], v[178:179] op_sel:[0,1,0] op_sel_hi:[1,0,1]
	v_pk_fma_f32 v[186:187], v[166:167], v[62:63], v[186:187] op_sel_hi:[0,1,1]
	v_pk_fma_f32 v[78:79], v[72:73], v[78:79], v[178:179]
	v_pk_fma_f32 v[188:189], v[166:167], v[48:49], v[188:189] op_sel:[1,0,0]
	ds_write_b32 v94, v79 offset:3168
	ds_write_b32 v94, v78 offset:3424
	v_pk_fma_f32 v[190:191], v[168:169], v[52:53], v[190:191] op_sel_hi:[0,1,1]
	v_pk_fma_f32 v[192:193], v[168:169], v[50:51], v[192:193] op_sel:[1,0,0]
	v_pk_fma_f32 v[186:187], v[170:171], v[54:55], v[186:187] op_sel_hi:[0,1,1]
	v_pk_fma_f32 v[188:189], v[170:171], v[40:41], v[188:189] op_sel:[1,0,0]
	v_pk_fma_f32 v[190:191], v[172:173], v[44:45], v[190:191] op_sel_hi:[0,1,1]
	v_pk_fma_f32 v[192:193], v[172:173], v[42:43], v[192:193] op_sel:[1,0,0]
	v_pk_fma_f32 v[186:187], v[174:175], v[46:47], v[186:187] op_sel_hi:[0,1,1]
	v_pk_fma_f32 v[188:189], v[174:175], v[24:25], v[188:189] op_sel:[1,0,0]
	v_pk_fma_f32 v[190:191], v[176:177], v[36:37], v[190:191] op_sel_hi:[0,1,1]
	v_pk_fma_f32 v[192:193], v[176:177], v[26:27], v[192:193] op_sel:[1,0,0]
	ds_read_b128 v[162:165], v133 offset:576
	ds_read_b128 v[166:169], v133 offset:592
	ds_read_b128 v[170:173], v133 offset:608
	ds_read_b128 v[174:177], v133 offset:624
	s_waitcnt lgkmcnt(4)
	v_pk_fma_f32 v[178:179], v[146:147], v[76:77], 0 op_sel_hi:[0,1,0]
	v_pk_add_f32 v[186:187], v[186:187], v[188:189]
	v_pk_fma_f32 v[180:181], v[146:147], v[56:57], 0 op_sel:[1,0,0] op_sel_hi:[1,1,0]
	v_pk_add_f32 v[190:191], v[190:191], v[192:193]
	v_pk_fma_f32 v[182:183], v[148:149], v[60:61], 0 op_sel_hi:[0,1,0]
	v_pk_add_f32 v[186:187], v[186:187], v[190:191]
	v_pk_fma_f32 v[184:185], v[148:149], v[58:59], 0 op_sel:[1,0,0] op_sel_hi:[1,1,0]
	v_pk_fma_f32 v[186:187], v[74:75], v[78:79], v[186:187] op_sel:[0,1,0] op_sel_hi:[1,0,1]
	v_pk_fma_f32 v[178:179], v[150:151], v[62:63], v[178:179] op_sel_hi:[0,1,1]
	v_pk_fma_f32 v[78:79], v[72:73], v[78:79], v[186:187]
	v_pk_fma_f32 v[180:181], v[150:151], v[48:49], v[180:181] op_sel:[1,0,0]
	ds_write_b32 v94, v79 offset:3696
	ds_write_b32 v94, v78 offset:3952
	v_pk_fma_f32 v[182:183], v[152:153], v[52:53], v[182:183] op_sel_hi:[0,1,1]
	v_pk_fma_f32 v[184:185], v[152:153], v[50:51], v[184:185] op_sel:[1,0,0]
	v_pk_fma_f32 v[178:179], v[154:155], v[54:55], v[178:179] op_sel_hi:[0,1,1]
	v_pk_fma_f32 v[180:181], v[154:155], v[40:41], v[180:181] op_sel:[1,0,0]
	v_pk_fma_f32 v[182:183], v[156:157], v[44:45], v[182:183] op_sel_hi:[0,1,1]
	v_pk_fma_f32 v[184:185], v[156:157], v[42:43], v[184:185] op_sel:[1,0,0]
	v_pk_fma_f32 v[178:179], v[158:159], v[46:47], v[178:179] op_sel_hi:[0,1,1]
	v_pk_fma_f32 v[180:181], v[158:159], v[24:25], v[180:181] op_sel:[1,0,0]
	v_pk_fma_f32 v[182:183], v[160:161], v[36:37], v[182:183] op_sel_hi:[0,1,1]
	v_pk_fma_f32 v[184:185], v[160:161], v[26:27], v[184:185] op_sel:[1,0,0]
	ds_read_b128 v[146:149], v133 offset:640
	ds_read_b128 v[150:153], v133 offset:656
	ds_read_b128 v[154:157], v133 offset:672
	ds_read_b128 v[158:161], v133 offset:688
	s_waitcnt lgkmcnt(4)
	v_pk_fma_f32 v[186:187], v[162:163], v[76:77], 0 op_sel_hi:[0,1,0]
	v_pk_add_f32 v[178:179], v[178:179], v[180:181]
	v_pk_fma_f32 v[188:189], v[162:163], v[56:57], 0 op_sel:[1,0,0] op_sel_hi:[1,1,0]
	v_pk_add_f32 v[182:183], v[182:183], v[184:185]
	v_pk_fma_f32 v[190:191], v[164:165], v[60:61], 0 op_sel_hi:[0,1,0]
	v_pk_add_f32 v[178:179], v[178:179], v[182:183]
	v_pk_fma_f32 v[192:193], v[164:165], v[58:59], 0 op_sel:[1,0,0] op_sel_hi:[1,1,0]
	v_pk_fma_f32 v[178:179], v[74:75], v[78:79], v[178:179] op_sel:[0,1,0] op_sel_hi:[1,0,1]
	v_pk_fma_f32 v[186:187], v[166:167], v[62:63], v[186:187] op_sel_hi:[0,1,1]
	v_pk_fma_f32 v[78:79], v[72:73], v[78:79], v[178:179]
	v_pk_fma_f32 v[188:189], v[166:167], v[48:49], v[188:189] op_sel:[1,0,0]
	ds_write_b32 v94, v79 offset:4224
	ds_write_b32 v94, v78 offset:4480
	v_pk_fma_f32 v[190:191], v[168:169], v[52:53], v[190:191] op_sel_hi:[0,1,1]
	v_pk_fma_f32 v[192:193], v[168:169], v[50:51], v[192:193] op_sel:[1,0,0]
	v_pk_fma_f32 v[186:187], v[170:171], v[54:55], v[186:187] op_sel_hi:[0,1,1]
	v_pk_fma_f32 v[188:189], v[170:171], v[40:41], v[188:189] op_sel:[1,0,0]
	v_pk_fma_f32 v[190:191], v[172:173], v[44:45], v[190:191] op_sel_hi:[0,1,1]
	v_pk_fma_f32 v[192:193], v[172:173], v[42:43], v[192:193] op_sel:[1,0,0]
	v_pk_fma_f32 v[186:187], v[174:175], v[46:47], v[186:187] op_sel_hi:[0,1,1]
	v_pk_fma_f32 v[188:189], v[174:175], v[24:25], v[188:189] op_sel:[1,0,0]
	v_pk_fma_f32 v[190:191], v[176:177], v[36:37], v[190:191] op_sel_hi:[0,1,1]
	v_pk_fma_f32 v[192:193], v[176:177], v[26:27], v[192:193] op_sel:[1,0,0]
	ds_read_b128 v[162:165], v133 offset:704
	ds_read_b128 v[166:169], v133 offset:720
	ds_read_b128 v[170:173], v133 offset:736
	ds_read_b128 v[174:177], v133 offset:752
	s_waitcnt lgkmcnt(4)
	v_pk_fma_f32 v[178:179], v[146:147], v[76:77], 0 op_sel_hi:[0,1,0]
	v_pk_add_f32 v[186:187], v[186:187], v[188:189]
	v_pk_fma_f32 v[180:181], v[146:147], v[56:57], 0 op_sel:[1,0,0] op_sel_hi:[1,1,0]
	v_pk_add_f32 v[190:191], v[190:191], v[192:193]
	v_pk_fma_f32 v[182:183], v[148:149], v[60:61], 0 op_sel_hi:[0,1,0]
	v_pk_add_f32 v[186:187], v[186:187], v[190:191]
	v_pk_fma_f32 v[184:185], v[148:149], v[58:59], 0 op_sel:[1,0,0] op_sel_hi:[1,1,0]
	v_pk_fma_f32 v[186:187], v[74:75], v[78:79], v[186:187] op_sel:[0,1,0] op_sel_hi:[1,0,1]
	v_pk_fma_f32 v[178:179], v[150:151], v[62:63], v[178:179] op_sel_hi:[0,1,1]
	v_pk_fma_f32 v[78:79], v[72:73], v[78:79], v[186:187]
	v_pk_fma_f32 v[180:181], v[150:151], v[48:49], v[180:181] op_sel:[1,0,0]
	ds_write_b32 v94, v79 offset:4752
	ds_write_b32 v94, v78 offset:5008
	v_pk_fma_f32 v[182:183], v[152:153], v[52:53], v[182:183] op_sel_hi:[0,1,1]
	v_pk_fma_f32 v[184:185], v[152:153], v[50:51], v[184:185] op_sel:[1,0,0]
	v_pk_fma_f32 v[178:179], v[154:155], v[54:55], v[178:179] op_sel_hi:[0,1,1]
	v_pk_fma_f32 v[180:181], v[154:155], v[40:41], v[180:181] op_sel:[1,0,0]
	v_pk_fma_f32 v[182:183], v[156:157], v[44:45], v[182:183] op_sel_hi:[0,1,1]
	v_pk_fma_f32 v[184:185], v[156:157], v[42:43], v[184:185] op_sel:[1,0,0]
	v_pk_fma_f32 v[178:179], v[158:159], v[46:47], v[178:179] op_sel_hi:[0,1,1]
	v_pk_fma_f32 v[180:181], v[158:159], v[24:25], v[180:181] op_sel:[1,0,0]
	v_pk_fma_f32 v[182:183], v[160:161], v[36:37], v[182:183] op_sel_hi:[0,1,1]
	v_pk_fma_f32 v[184:185], v[160:161], v[26:27], v[184:185] op_sel:[1,0,0]
	ds_read_b128 v[146:149], v133 offset:768
	ds_read_b128 v[150:153], v133 offset:784
	ds_read_b128 v[154:157], v133 offset:800
	ds_read_b128 v[158:161], v133 offset:816
	s_waitcnt lgkmcnt(4)
	v_pk_fma_f32 v[186:187], v[162:163], v[76:77], 0 op_sel_hi:[0,1,0]
	v_pk_add_f32 v[178:179], v[178:179], v[180:181]
	v_pk_fma_f32 v[188:189], v[162:163], v[56:57], 0 op_sel:[1,0,0] op_sel_hi:[1,1,0]
	v_pk_add_f32 v[182:183], v[182:183], v[184:185]
	v_pk_fma_f32 v[190:191], v[164:165], v[60:61], 0 op_sel_hi:[0,1,0]
	v_pk_add_f32 v[178:179], v[178:179], v[182:183]
	v_pk_fma_f32 v[192:193], v[164:165], v[58:59], 0 op_sel:[1,0,0] op_sel_hi:[1,1,0]
	v_pk_fma_f32 v[178:179], v[74:75], v[78:79], v[178:179] op_sel:[0,1,0] op_sel_hi:[1,0,1]
	v_pk_fma_f32 v[186:187], v[166:167], v[62:63], v[186:187] op_sel_hi:[0,1,1]
	v_pk_fma_f32 v[78:79], v[72:73], v[78:79], v[178:179]
	v_pk_fma_f32 v[188:189], v[166:167], v[48:49], v[188:189] op_sel:[1,0,0]
	ds_write_b32 v94, v79 offset:5280
	ds_write_b32 v94, v78 offset:5536
	v_pk_fma_f32 v[190:191], v[168:169], v[52:53], v[190:191] op_sel_hi:[0,1,1]
	v_pk_fma_f32 v[192:193], v[168:169], v[50:51], v[192:193] op_sel:[1,0,0]
	v_pk_fma_f32 v[186:187], v[170:171], v[54:55], v[186:187] op_sel_hi:[0,1,1]
	v_pk_fma_f32 v[188:189], v[170:171], v[40:41], v[188:189] op_sel:[1,0,0]
	v_pk_fma_f32 v[190:191], v[172:173], v[44:45], v[190:191] op_sel_hi:[0,1,1]
	v_pk_fma_f32 v[192:193], v[172:173], v[42:43], v[192:193] op_sel:[1,0,0]
	v_pk_fma_f32 v[186:187], v[174:175], v[46:47], v[186:187] op_sel_hi:[0,1,1]
	v_pk_fma_f32 v[188:189], v[174:175], v[24:25], v[188:189] op_sel:[1,0,0]
	v_pk_fma_f32 v[190:191], v[176:177], v[36:37], v[190:191] op_sel_hi:[0,1,1]
	v_pk_fma_f32 v[192:193], v[176:177], v[26:27], v[192:193] op_sel:[1,0,0]
	ds_read_b128 v[162:165], v133 offset:832
	ds_read_b128 v[166:169], v133 offset:848
	ds_read_b128 v[170:173], v133 offset:864
	ds_read_b128 v[174:177], v133 offset:880
	s_waitcnt lgkmcnt(4)
	v_pk_fma_f32 v[178:179], v[146:147], v[76:77], 0 op_sel_hi:[0,1,0]
	v_pk_add_f32 v[186:187], v[186:187], v[188:189]
	v_pk_fma_f32 v[180:181], v[146:147], v[56:57], 0 op_sel:[1,0,0] op_sel_hi:[1,1,0]
	v_pk_add_f32 v[190:191], v[190:191], v[192:193]
	v_pk_fma_f32 v[182:183], v[148:149], v[60:61], 0 op_sel_hi:[0,1,0]
	v_pk_add_f32 v[186:187], v[186:187], v[190:191]
	v_pk_fma_f32 v[184:185], v[148:149], v[58:59], 0 op_sel:[1,0,0] op_sel_hi:[1,1,0]
	v_pk_fma_f32 v[186:187], v[74:75], v[78:79], v[186:187] op_sel:[0,1,0] op_sel_hi:[1,0,1]
	v_pk_fma_f32 v[178:179], v[150:151], v[62:63], v[178:179] op_sel_hi:[0,1,1]
	v_pk_fma_f32 v[78:79], v[72:73], v[78:79], v[186:187]
	v_pk_fma_f32 v[180:181], v[150:151], v[48:49], v[180:181] op_sel:[1,0,0]
	ds_write_b32 v94, v79 offset:5808
	ds_write_b32 v94, v78 offset:6064
	v_pk_fma_f32 v[182:183], v[152:153], v[52:53], v[182:183] op_sel_hi:[0,1,1]
	v_pk_fma_f32 v[184:185], v[152:153], v[50:51], v[184:185] op_sel:[1,0,0]
	v_pk_fma_f32 v[178:179], v[154:155], v[54:55], v[178:179] op_sel_hi:[0,1,1]
	v_pk_fma_f32 v[180:181], v[154:155], v[40:41], v[180:181] op_sel:[1,0,0]
	v_pk_fma_f32 v[182:183], v[156:157], v[44:45], v[182:183] op_sel_hi:[0,1,1]
	v_pk_fma_f32 v[184:185], v[156:157], v[42:43], v[184:185] op_sel:[1,0,0]
	v_pk_fma_f32 v[178:179], v[158:159], v[46:47], v[178:179] op_sel_hi:[0,1,1]
	v_pk_fma_f32 v[180:181], v[158:159], v[24:25], v[180:181] op_sel:[1,0,0]
	v_pk_fma_f32 v[182:183], v[160:161], v[36:37], v[182:183] op_sel_hi:[0,1,1]
	v_pk_fma_f32 v[184:185], v[160:161], v[26:27], v[184:185] op_sel:[1,0,0]
	ds_read_b128 v[146:149], v133 offset:896
	ds_read_b128 v[150:153], v133 offset:912
	ds_read_b128 v[154:157], v133 offset:928
	ds_read_b128 v[158:161], v133 offset:944
	s_waitcnt lgkmcnt(4)
	v_pk_fma_f32 v[186:187], v[162:163], v[76:77], 0 op_sel_hi:[0,1,0]
	v_pk_add_f32 v[178:179], v[178:179], v[180:181]
	v_pk_fma_f32 v[188:189], v[162:163], v[56:57], 0 op_sel:[1,0,0] op_sel_hi:[1,1,0]
	v_pk_add_f32 v[182:183], v[182:183], v[184:185]
	v_pk_fma_f32 v[190:191], v[164:165], v[60:61], 0 op_sel_hi:[0,1,0]
	v_pk_add_f32 v[178:179], v[178:179], v[182:183]
	v_pk_fma_f32 v[192:193], v[164:165], v[58:59], 0 op_sel:[1,0,0] op_sel_hi:[1,1,0]
	v_pk_fma_f32 v[178:179], v[74:75], v[78:79], v[178:179] op_sel:[0,1,0] op_sel_hi:[1,0,1]
	v_pk_fma_f32 v[186:187], v[166:167], v[62:63], v[186:187] op_sel_hi:[0,1,1]
	v_pk_fma_f32 v[78:79], v[72:73], v[78:79], v[178:179]
	v_pk_fma_f32 v[188:189], v[166:167], v[48:49], v[188:189] op_sel:[1,0,0]
	ds_write_b32 v94, v79 offset:6336
	ds_write_b32 v94, v78 offset:6592
	v_pk_fma_f32 v[190:191], v[168:169], v[52:53], v[190:191] op_sel_hi:[0,1,1]
	v_pk_fma_f32 v[192:193], v[168:169], v[50:51], v[192:193] op_sel:[1,0,0]
	v_pk_fma_f32 v[186:187], v[170:171], v[54:55], v[186:187] op_sel_hi:[0,1,1]
	v_pk_fma_f32 v[188:189], v[170:171], v[40:41], v[188:189] op_sel:[1,0,0]
	v_pk_fma_f32 v[190:191], v[172:173], v[44:45], v[190:191] op_sel_hi:[0,1,1]
	v_pk_fma_f32 v[192:193], v[172:173], v[42:43], v[192:193] op_sel:[1,0,0]
	v_pk_fma_f32 v[186:187], v[174:175], v[46:47], v[186:187] op_sel_hi:[0,1,1]
	v_pk_fma_f32 v[188:189], v[174:175], v[24:25], v[188:189] op_sel:[1,0,0]
	v_pk_fma_f32 v[190:191], v[176:177], v[36:37], v[190:191] op_sel_hi:[0,1,1]
	v_pk_fma_f32 v[192:193], v[176:177], v[26:27], v[192:193] op_sel:[1,0,0]
	ds_read_b128 v[162:165], v133 offset:960
	ds_read_b128 v[166:169], v133 offset:976
	ds_read_b128 v[170:173], v133 offset:992
	ds_read_b128 v[174:177], v133 offset:1008
	s_waitcnt lgkmcnt(4)
	v_pk_fma_f32 v[178:179], v[146:147], v[76:77], 0 op_sel_hi:[0,1,0]
	v_pk_add_f32 v[186:187], v[186:187], v[188:189]
	v_pk_fma_f32 v[180:181], v[146:147], v[56:57], 0 op_sel:[1,0,0] op_sel_hi:[1,1,0]
	v_pk_add_f32 v[190:191], v[190:191], v[192:193]
	v_pk_fma_f32 v[182:183], v[148:149], v[60:61], 0 op_sel_hi:[0,1,0]
	v_pk_add_f32 v[186:187], v[186:187], v[190:191]
	v_pk_fma_f32 v[184:185], v[148:149], v[58:59], 0 op_sel:[1,0,0] op_sel_hi:[1,1,0]
	v_pk_fma_f32 v[186:187], v[74:75], v[78:79], v[186:187] op_sel:[0,1,0] op_sel_hi:[1,0,1]
	v_pk_fma_f32 v[178:179], v[150:151], v[62:63], v[178:179] op_sel_hi:[0,1,1]
	v_pk_fma_f32 v[78:79], v[72:73], v[78:79], v[186:187]
	v_pk_fma_f32 v[180:181], v[150:151], v[48:49], v[180:181] op_sel:[1,0,0]
	ds_write_b32 v94, v79 offset:6864
	ds_write_b32 v94, v78 offset:7120
	v_pk_fma_f32 v[182:183], v[152:153], v[52:53], v[182:183] op_sel_hi:[0,1,1]
	v_pk_fma_f32 v[184:185], v[152:153], v[50:51], v[184:185] op_sel:[1,0,0]
	v_pk_fma_f32 v[178:179], v[154:155], v[54:55], v[178:179] op_sel_hi:[0,1,1]
	v_pk_fma_f32 v[180:181], v[154:155], v[40:41], v[180:181] op_sel:[1,0,0]
	v_pk_fma_f32 v[182:183], v[156:157], v[44:45], v[182:183] op_sel_hi:[0,1,1]
	v_pk_fma_f32 v[184:185], v[156:157], v[42:43], v[184:185] op_sel:[1,0,0]
	v_pk_fma_f32 v[178:179], v[158:159], v[46:47], v[178:179] op_sel_hi:[0,1,1]
	v_pk_fma_f32 v[180:181], v[158:159], v[24:25], v[180:181] op_sel:[1,0,0]
	v_pk_fma_f32 v[182:183], v[160:161], v[36:37], v[182:183] op_sel_hi:[0,1,1]
	v_pk_fma_f32 v[184:185], v[160:161], v[26:27], v[184:185] op_sel:[1,0,0]
	s_waitcnt lgkmcnt(2)
	v_pk_fma_f32 v[186:187], v[162:163], v[76:77], 0 op_sel_hi:[0,1,0]
	v_pk_add_f32 v[178:179], v[178:179], v[180:181]
	v_pk_fma_f32 v[188:189], v[162:163], v[56:57], 0 op_sel:[1,0,0] op_sel_hi:[1,1,0]
	v_pk_add_f32 v[182:183], v[182:183], v[184:185]
	v_pk_fma_f32 v[190:191], v[164:165], v[60:61], 0 op_sel_hi:[0,1,0]
	v_pk_add_f32 v[178:179], v[178:179], v[182:183]
	v_pk_fma_f32 v[192:193], v[164:165], v[58:59], 0 op_sel:[1,0,0] op_sel_hi:[1,1,0]
	v_pk_fma_f32 v[178:179], v[74:75], v[78:79], v[178:179] op_sel:[0,1,0] op_sel_hi:[1,0,1]
	v_pk_fma_f32 v[186:187], v[166:167], v[62:63], v[186:187] op_sel_hi:[0,1,1]
	v_pk_fma_f32 v[78:79], v[72:73], v[78:79], v[178:179]
	v_pk_fma_f32 v[188:189], v[166:167], v[48:49], v[188:189] op_sel:[1,0,0]
	ds_write_b32 v94, v79 offset:7392
	ds_write_b32 v94, v78 offset:7648
	v_pk_fma_f32 v[190:191], v[168:169], v[52:53], v[190:191] op_sel_hi:[0,1,1]
	v_pk_fma_f32 v[192:193], v[168:169], v[50:51], v[192:193] op_sel:[1,0,0]
	v_pk_fma_f32 v[186:187], v[170:171], v[54:55], v[186:187] op_sel_hi:[0,1,1]
	v_pk_fma_f32 v[188:189], v[170:171], v[40:41], v[188:189] op_sel:[1,0,0]
	v_pk_fma_f32 v[190:191], v[172:173], v[44:45], v[190:191] op_sel_hi:[0,1,1]
	v_pk_fma_f32 v[192:193], v[172:173], v[42:43], v[192:193] op_sel:[1,0,0]
	v_pk_fma_f32 v[186:187], v[174:175], v[46:47], v[186:187] op_sel_hi:[0,1,1]
	v_pk_fma_f32 v[188:189], v[174:175], v[24:25], v[188:189] op_sel:[1,0,0]
	v_pk_fma_f32 v[190:191], v[176:177], v[36:37], v[190:191] op_sel_hi:[0,1,1]
	v_pk_fma_f32 v[192:193], v[176:177], v[26:27], v[192:193] op_sel:[1,0,0]
	v_pk_add_f32 v[186:187], v[186:187], v[188:189]
	v_pk_add_f32 v[190:191], v[190:191], v[192:193]
	s_nop 0
	v_pk_add_f32 v[186:187], v[186:187], v[190:191]
	s_nop 0
	v_pk_fma_f32 v[186:187], v[74:75], v[78:79], v[186:187] op_sel:[0,1,0] op_sel_hi:[1,0,1]
	s_nop 0
	v_pk_fma_f32 v[78:79], v[72:73], v[78:79], v[186:187]
	s_nop 0
	ds_write_b32 v94, v79 offset:7920
	ds_write_b32 v94, v78 offset:8176
	s_waitcnt lgkmcnt(0)
	ds_read_b128 v[80:83], v99
	ds_read_b128 v[106:109], v99 offset:16
	v_lshl_or_b32 v7, s0, 4, v95
	v_or_b32_e32 v4, v8, v7
	v_lshl_add_u32 v10, v7, 5, v96
	s_waitcnt lgkmcnt(1)
	v_mfma_f32_16x16x4_f32 v[110:113], v80, v32, 0
	v_or_b32_e32 v71, 1, v7
	v_or_b32_e32 v105, 2, v7
	v_or_b32_e32 v7, 3, v7
	v_or_b32_e32 v114, v8, v105
	v_lshl_add_u32 v105, v105, 5, v96
	v_or_b32_e32 v116, v8, v7
	v_lshl_add_u32 v7, v7, 5, v96
	v_mfma_f32_16x16x4_f32 v[110:113], v81, v33, v[110:113]
	v_mov_b32_e32 v5, v9
	v_mov_b32_e32 v11, v9
	v_mov_b32_e32 v115, v9
	v_mov_b32_e32 v117, v9
	s_add_i32 s0, s0, 1
	v_mad_u64_u32 v[118:119], s[4:5], v114, s95, v[0:1]
	v_mfma_f32_16x16x4_f32 v[110:113], v82, v34, v[110:113]
	s_cmp_eq_u32 s0, 4
	v_lshlrev_b64 v[114:115], 10, v[114:115]
	v_mad_i32_i24 v119, v9, s95, v119
	v_add_u32_e32 v6, 0x200, v6
	v_lshl_add_u64 v[114:115], v[2:3], 0, v[114:115]
	v_mfma_f32_16x16x4_f32 v[80:83], v83, v35, v[110:113]
	s_waitcnt lgkmcnt(0)
	v_mfma_f32_16x16x4_f32 v[80:83], v106, v28, v[80:83]
	v_mfma_f32_16x16x4_f32 v[80:83], v107, v29, v[80:83]
	v_mfma_f32_16x16x4_f32 v[80:83], v108, v30, v[80:83]
	v_mfma_f32_16x16x4_f32 v[80:83], v109, v31, v[80:83]
	ds_read_b128 v[106:109], v99 offset:32
	ds_read_b128 v[110:113], v99 offset:48
	s_waitcnt lgkmcnt(1)
	v_mfma_f32_16x16x4_f32 v[80:83], v106, v20, v[80:83]
	v_mfma_f32_16x16x4_f32 v[80:83], v107, v21, v[80:83]
	v_mfma_f32_16x16x4_f32 v[80:83], v108, v22, v[80:83]
	v_mfma_f32_16x16x4_f32 v[80:83], v109, v23, v[80:83]
	s_waitcnt lgkmcnt(0)
	v_mfma_f32_16x16x4_f32 v[80:83], v110, v16, v[80:83]
	v_mfma_f32_16x16x4_f32 v[80:83], v111, v17, v[80:83]
	v_mfma_f32_16x16x4_f32 v[80:83], v112, v18, v[80:83]
	v_mfma_f32_16x16x4_f32 v[80:83], v113, v19, v[80:83]
	ds_read_b128 v[106:109], v99 offset:64
	ds_read_b128 v[110:113], v99 offset:80
	s_waitcnt lgkmcnt(1)
	v_mfma_f32_16x16x4_f32 v[80:83], v106, v12, v[80:83]
	v_mfma_f32_16x16x4_f32 v[80:83], v107, v13, v[80:83]
	v_mfma_f32_16x16x4_f32 v[80:83], v108, v14, v[80:83]
	v_mfma_f32_16x16x4_f32 v[80:83], v109, v15, v[80:83]
	s_waitcnt lgkmcnt(0)
	v_mfma_f32_16x16x4_f32 v[80:83], v110, v38, v[80:83]
	v_mfma_f32_16x16x4_f32 v[80:83], v111, v39, v[80:83]
	v_mfma_f32_16x16x4_f32 v[80:83], v112, v84, v[80:83]
	v_mfma_f32_16x16x4_f32 v[80:83], v113, v85, v[80:83]
	ds_read_b128 v[106:109], v99 offset:96
	ds_read_b128 v[110:113], v99 offset:112
	s_waitcnt lgkmcnt(0)
	ds_read_u16 v120, v10
	v_or_b32_e32 v10, v8, v71
	v_lshl_add_u32 v71, v71, 5, v96
	ds_read_u16 v71, v71
	ds_read_u16 v105, v105
	s_waitcnt lgkmcnt(4)
	v_mfma_f32_16x16x4_f32 v[80:83], v106, v86, v[80:83]
	ds_read_u16 v7, v7
	s_waitcnt lgkmcnt(2)
	v_lshlrev_b32_e32 v71, 16, v71
	s_waitcnt lgkmcnt(1)
	v_lshlrev_b32_e32 v105, 16, v105
	s_waitcnt lgkmcnt(0)
	v_lshlrev_b32_e32 v7, 16, v7
	v_mfma_f32_16x16x4_f32 v[80:83], v107, v87, v[80:83]
	v_mad_u64_u32 v[106:107], s[4:5], v4, s95, v[0:1]
	v_lshlrev_b64 v[4:5], 10, v[4:5]
	v_mad_i32_i24 v107, v9, s95, v107
	v_lshl_add_u64 v[4:5], v[2:3], 0, v[4:5]
	v_mfma_f32_16x16x4_f32 v[80:83], v108, v88, v[80:83]
	v_mfma_f32_16x16x4_f32 v[80:83], v109, v89, v[80:83]
	v_mad_u64_u32 v[108:109], s[4:5], v10, s95, v[0:1]
	v_lshlrev_b64 v[10:11], 10, v[10:11]
	v_mad_i32_i24 v109, v9, s95, v109
	v_lshl_add_u64 v[10:11], v[2:3], 0, v[10:11]
	v_mfma_f32_16x16x4_f32 v[80:83], v110, v101, v[80:83]
	v_mfma_f32_16x16x4_f32 v[80:83], v111, v102, v[80:83]
	v_mad_u64_u32 v[110:111], s[4:5], v116, s95, v[0:1]
	v_lshlrev_b64 v[116:117], 10, v[116:117]
	v_mad_i32_i24 v111, v9, s95, v111
	v_lshl_add_u64 v[116:117], v[2:3], 0, v[116:117]
	v_mfma_f32_16x16x4_f32 v[80:83], v112, v103, v[80:83]
	v_lshlrev_b32_e32 v112, 16, v120
	v_mfma_f32_16x16x4_f32 v[80:83], v113, v104, v[80:83]
	s_nop 9
	v_fma_f32 v80, v100, v112, v80
	v_fma_f32 v71, v100, v71, v81
	v_fma_f32 v81, v100, v105, v82
	v_fmac_f32_e32 v83, v100, v7
	v_mul_f32_e32 v7, 0x3d372713, v80
	v_mul_f32_e32 v82, 0x3d372713, v71
	v_mul_f32_e32 v105, 0x3d372713, v81
	v_mul_f32_e32 v112, 0x3d372713, v83
	v_mul_f32_e32 v7, v80, v7
	v_mul_f32_e32 v82, v71, v82
	v_mul_f32_e32 v105, v81, v105
	v_mul_f32_e32 v112, v83, v112
	v_fma_f32 v7, v80, v7, v80
	v_fma_f32 v82, v71, v82, v71
	v_fma_f32 v105, v81, v105, v81
	v_fma_f32 v112, v83, v112, v83
	v_mul_f32_e32 v7, 0xbfcc422a, v7
	v_mul_f32_e32 v82, 0xbfcc422a, v82
	v_mul_f32_e32 v105, 0xbfcc422a, v105
	v_mul_f32_e32 v112, 0xbfcc422a, v112
	v_mul_f32_e32 v7, 0x3fb8aa3b, v7
	v_mul_f32_e32 v82, 0x3fb8aa3b, v82
	v_mul_f32_e32 v105, 0x3fb8aa3b, v105
	v_mul_f32_e32 v112, 0x3fb8aa3b, v112
	v_exp_f32_e32 v7, v7
	v_exp_f32_e32 v82, v82
	v_exp_f32_e32 v105, v105
	v_exp_f32_e32 v112, v112
	v_add_f32_e32 v7, 1.0, v7
	v_add_f32_e32 v82, 1.0, v82
	v_add_f32_e32 v105, 1.0, v105
	v_add_f32_e32 v112, 1.0, v112
	v_rcp_f32_e32 v7, v7
	v_rcp_f32_e32 v82, v82
	v_rcp_f32_e32 v105, v105
	v_rcp_f32_e32 v112, v112
	v_mul_f32_e32 v7, v80, v7
	v_mul_f32_e32 v71, v71, v82
	v_mul_f32_e32 v80, v81, v105
	v_mul_f32_e32 v81, v83, v112
	v_bfe_u32 v82, v7, 16, 1
	global_store_dword v[106:107], v7, off
	v_bfe_u32 v83, v71, 16, 1
	v_bfe_u32 v105, v80, 16, 1
	v_bfe_u32 v106, v81, 16, 1
	v_add3_u32 v7, v7, v82, s96
	global_store_dword v[108:109], v71, off
	global_store_dword v[118:119], v80, off
	global_store_dword v[110:111], v81, off
	v_add3_u32 v71, v71, v83, s96
	v_add3_u32 v80, v80, v105, s96
	v_add3_u32 v81, v81, v106, s96
	global_store_short_d16_hi v[4:5], v7, off
	global_store_short_d16_hi v[10:11], v71, off
	global_store_short_d16_hi v[114:115], v80, off
	global_store_short_d16_hi v[116:117], v81, off
	s_cbranch_scc0 .LBB0_532
	v_lshrrev_b32_e32 v0, 3, v90
	v_and_b32_e32 v1, 7, v90
	v_lshl_add_u32 v0, v0, 2, v1
	v_add_u32_e32 v0, 0xa00, v0
	v_add_u32_e32 v2, 0x800, v90
	s_movk_i32 s0, 0x3ff
	v_cmp_lt_i32_e32 vcc, s0, v90
	v_cmp_lt_u32_e64 s[0:1], 3, v1
	s_nop 1
	v_cndmask_b32_e32 v0, v2, v0, vcc
	s_and_b64 s[0:1], s[0:1], vcc
	s_movk_i32 s2, 0x7ff
	v_cmp_lt_i32_e32 vcc, s2, v90
	s_nop 1
	s_or_b64 vcc, vcc, s[0:1]
	s_or_b64 s[26:27], vcc, s[26:27]
	v_mov_b32_e32 v90, v0
	s_andn2_b64 exec, exec, s[26:27]
	s_cbranch_execnz .LBB0_519
